# GEMM loop code placement: every iteration padded to a multiple of 8 bytes and the loop placed so its 8-byte instructions (MFMA/ds_read/DMA) sit at offsets 4 mod 8 (the 0 mod 8 placement measured 1.1 u
# baseline (speedup 1.0000x reference)
_Z8gemm_qkvPKDF16_S0_PKfPDF16_S3_S3_Pj:
	v_readfirstlane_b32 s13, v0
	s_lshr_b32 s8, s13, 6
	v_bfe_u32 v2, v0, 3, 3
	s_load_dwordx4 s[4:7], s[0:1], 0x0
	v_lshl_or_b32 v6, s8, 3, v2
	v_lshrrev_b32_e32 v2, 1, v6
	s_mul_i32 s16, s3, 0xc0
	v_xor_b32_e32 v4, v2, v0
	v_add_u32_e32 v2, s16, v6
	v_ashrrev_i32_e32 v3, 31, v2
	s_bfe_u32 s15, s13, 0x20006
	v_lshlrev_b64 v[2:3], 11, v[2:3]
	v_lshlrev_b32_e32 v4, 4, v4
	s_mul_i32 s10, s2, 0xc0
	s_mul_i32 s2, s15, 48
	s_waitcnt lgkmcnt(0)
	v_lshl_add_u64 v[2:3], s[4:5], 0, v[2:3]
	v_and_b32_e32 v4, 0x70, v4
	v_mov_b32_e32 v5, 0
	s_add_i32 s17, s2, s10
	v_lshl_add_u64 v[218:219], v[2:3], 0, v[4:5]
	v_add_u32_e32 v2, s10, v6
	s_lshl_b32 s8, s8, 10
	v_ashrrev_i32_e32 v3, 31, v2
	s_cmp_lg_u32 0x400, -1
	v_lshlrev_b64 v[2:3], 11, v[2:3]
	s_cselect_b32 s4, 0x400, 0
	v_lshl_add_u64 v[2:3], s[6:7], 0, v[2:3]
	s_add_i32 s11, s8, s4
	s_mov_b32 s4, m0
	s_mov_b32 m0, s11
	s_nop 0
	global_load_lds_dwordx4 v[218:219], off
	s_mov_b32 m0, s4
	v_lshl_add_u64 v[220:221], v[2:3], 0, v[4:5]
	s_add_i32 s4, s11, 0x6000
	s_mov_b32 s5, m0
	s_mov_b32 m0, s4
	s_nop 0
	global_load_lds_dwordx4 v[220:221], off
	s_mov_b32 m0, s5
	s_mov_b64 s[4:5], 0x20000
	v_lshl_add_u64 v[222:223], v[218:219], 0, s[4:5]
	s_add_i32 s9, s11, 0x2000
	s_mov_b32 s6, m0
	s_mov_b32 m0, s9
	s_nop 0
	global_load_lds_dwordx4 v[222:223], off
	s_mov_b32 m0, s6
	v_lshl_add_u64 v[224:225], v[220:221], 0, s[4:5]
	s_add_i32 s4, s11, 0x8000
	s_mov_b32 s5, m0
	s_mov_b32 m0, s4
	s_nop 0
	global_load_lds_dwordx4 v[224:225], off
	s_mov_b32 m0, s5
	s_mov_b64 s[4:5], 0x40000
	v_lshl_add_u64 v[226:227], v[218:219], 0, s[4:5]
	s_add_i32 s12, s11, 0x4000
	s_mov_b32 s6, m0
	s_mov_b32 m0, s12
	s_nop 0
	global_load_lds_dwordx4 v[226:227], off
	s_mov_b32 m0, s6
	v_lshl_add_u64 v[228:229], v[220:221], 0, s[4:5]
	s_add_i32 s4, s11, 0xa000
	s_mov_b32 s5, m0
	s_mov_b32 m0, s4
	s_nop 0
	global_load_lds_dwordx4 v[228:229], off
	s_mov_b32 m0, s5
	s_cmpk_gt_i32 s17, 0x7d0
	s_cselect_b64 s[4:5], -1, 0
	s_lshr_b32 s14, s13, 8
	s_mul_i32 s6, s14, 0x3000
	s_add_i32 s13, s6, 0x400
	s_mov_b64 s[6:7], 0x80
	s_add_i32 s18, s11, 0xc000
	v_lshl_add_u64 v[2:3], v[218:219], 0, s[6:7]
	s_mov_b32 s30, m0
	s_mov_b32 m0, s18
	s_nop 0
	global_load_lds_dwordx4 v[2:3], off
	s_mov_b32 m0, s30
	s_add_i32 s19, s11, 0x12000
	v_lshl_add_u64 v[2:3], v[220:221], 0, s[6:7]
	s_mov_b32 s6, m0
	s_mov_b32 m0, s19
	s_nop 0
	global_load_lds_dwordx4 v[2:3], off
	s_mov_b32 m0, s6
	s_mov_b64 s[6:7], 0x20080
	s_add_i32 s20, s11, 0xe000
	v_lshl_add_u64 v[2:3], v[218:219], 0, s[6:7]
	s_mov_b32 s18, m0
	s_mov_b32 m0, s20
	s_nop 0
	global_load_lds_dwordx4 v[2:3], off
	s_mov_b32 m0, s18
	s_add_i32 s21, s11, 0x14000
	v_lshl_add_u64 v[2:3], v[220:221], 0, s[6:7]
	s_mov_b32 s6, m0
	s_mov_b32 m0, s21
	s_nop 0
	global_load_lds_dwordx4 v[2:3], off
	s_mov_b32 m0, s6
	s_mov_b64 s[6:7], 0x40080
	v_lshl_add_u64 v[2:3], v[218:219], 0, s[6:7]
	s_add_i32 s22, s11, 0x10000
	s_mov_b32 s18, m0
	s_mov_b32 m0, s22
	s_nop 0
	global_load_lds_dwordx4 v[2:3], off
	s_mov_b32 m0, s18
	v_lshl_add_u64 v[2:3], v[220:221], 0, s[6:7]
	v_and_b32_e32 v1, 15, v0
	v_bfe_u32 v231, v0, 4, 2
	s_add_i32 s23, s11, 0x16000
	s_mov_b32 s6, m0
	s_mov_b32 m0, s23
	s_nop 0
	global_load_lds_dwordx4 v[2:3], off
	s_mov_b32 m0, s6
	v_lshrrev_b32_e32 v3, 1, v0
	v_lshlrev_b32_e32 v2, 7, v1
	v_bfe_u32 v4, v0, 1, 3
	v_bitop3_b32 v3, v231, v3, 7 bitop3:0x78
	v_lshl_or_b32 v238, v3, 4, v2
	v_bitop3_b32 v3, v231, v4, 4 bitop3:0x36
	v_lshl_or_b32 v240, v3, 4, v2
	s_mulk_i32 s15, 0x1800
	s_addk_i32 s15, 0x6400
	v_add_u32_e32 v158, s13, v238
	v_add_u32_e32 v160, s13, v240
	v_add_u32_e32 v162, s15, v238
	v_add_u32_e32 v164, s15, v240
	s_add_u32 m0, s11, 0x17f00
	s_nop 0
	global_load_lds_dwordx4 v[218:219], off offset:256
	s_add_u32 m0, s11, 0x19f00
	s_nop 0
	global_load_lds_dwordx4 v[222:223], off offset:256
	s_add_u32 m0, s11, 0x1bf00
	s_nop 0
	global_load_lds_dwordx4 v[226:227], off offset:256
	s_load_dwordx2 s[24:25], s[0:1], 0x10
	s_mov_b32 s20, 0x180
	s_mov_b32 s21, 0
	v_lshl_add_u64 v[218:219], v[218:219], 0, s[20:21]
	v_lshl_add_u64 v[222:223], v[222:223], 0, s[20:21]
	v_lshl_add_u64 v[226:227], v[226:227], 0, s[20:21]
	v_lshl_add_u64 v[220:221], v[220:221], 0, s[20:21]
	v_lshl_add_u64 v[224:225], v[224:225], 0, s[20:21]
	v_lshl_add_u64 v[228:229], v[228:229], 0, s[20:21]
	v_add_u32_e32 v159, 0x18000, v158
	v_add_u32_e32 v161, 0x18000, v160
	v_add_u32_e32 v163, 0x18000, v162
	v_add_u32_e32 v165, 0x18000, v164
	v_mov_b32_e32 v82, 0
	v_mov_b32_e32 v83, 0
	v_mov_b32_e32 v84, 0
	v_mov_b32_e32 v85, 0
	v_mov_b32_e32 v58, 0
	v_mov_b32_e32 v59, 0
	v_mov_b32_e32 v60, 0
	v_mov_b32_e32 v61, 0
	v_mov_b32_e32 v14, 0
	v_mov_b32_e32 v15, 0
	v_mov_b32_e32 v16, 0
	v_mov_b32_e32 v17, 0
	v_mov_b32_e32 v78, 0
	v_mov_b32_e32 v79, 0
	v_mov_b32_e32 v80, 0
	v_mov_b32_e32 v81, 0
	v_mov_b32_e32 v22, 0
	v_mov_b32_e32 v23, 0
	v_mov_b32_e32 v24, 0
	v_mov_b32_e32 v25, 0
	v_mov_b32_e32 v30, 0
	v_mov_b32_e32 v31, 0
	v_mov_b32_e32 v32, 0
	v_mov_b32_e32 v33, 0
	v_mov_b32_e32 v74, 0
	v_mov_b32_e32 v75, 0
	v_mov_b32_e32 v76, 0
	v_mov_b32_e32 v77, 0
	v_mov_b32_e32 v18, 0
	v_mov_b32_e32 v19, 0
	v_mov_b32_e32 v20, 0
	v_mov_b32_e32 v21, 0
	v_mov_b32_e32 v26, 0
	v_mov_b32_e32 v27, 0
	v_mov_b32_e32 v28, 0
	v_mov_b32_e32 v29, 0
	v_mov_b32_e32 v70, 0
	v_mov_b32_e32 v71, 0
	v_mov_b32_e32 v72, 0
	v_mov_b32_e32 v73, 0
	v_mov_b32_e32 v46, 0
	v_mov_b32_e32 v47, 0
	v_mov_b32_e32 v48, 0
	v_mov_b32_e32 v49, 0
	v_mov_b32_e32 v240, 0
	v_mov_b32_e32 v241, 0
	v_mov_b32_e32 v242, 0
	v_mov_b32_e32 v243, 0
	v_mov_b32_e32 v66, 0
	v_mov_b32_e32 v67, 0
	v_mov_b32_e32 v68, 0
	v_mov_b32_e32 v69, 0
	v_mov_b32_e32 v42, 0
	v_mov_b32_e32 v43, 0
	v_mov_b32_e32 v44, 0
	v_mov_b32_e32 v45, 0
	v_mov_b32_e32 v236, 0
	v_mov_b32_e32 v237, 0
	v_mov_b32_e32 v238, 0
	v_mov_b32_e32 v239, 0
	v_mov_b32_e32 v62, 0
	v_mov_b32_e32 v63, 0
	v_mov_b32_e32 v64, 0
	v_mov_b32_e32 v65, 0
	v_mov_b32_e32 v38, 0
	v_mov_b32_e32 v39, 0
	v_mov_b32_e32 v40, 0
	v_mov_b32_e32 v41, 0
	v_mov_b32_e32 v34, 0
	v_mov_b32_e32 v35, 0
	v_mov_b32_e32 v36, 0
	v_mov_b32_e32 v37, 0
	s_not_b64 s[6:7], s[4:5]
	s_mov_b32 s22, 4
	s_waitcnt vmcnt(9) lgkmcnt(0)
	s_barrier
	ds_read_b128 v[134:137], v162
	ds_read_b128 v[138:141], v162 offset:2048
	ds_read_b128 v[142:145], v162 offset:4096
	ds_read_b128 v[86:89], v158
	ds_read_b128 v[90:93], v158 offset:2048
	ds_read_b128 v[94:97], v158 offset:4096
	ds_read_b128 v[98:101], v158 offset:6144
	ds_read_b128 v[102:105], v158 offset:8192
	ds_read_b128 v[106:109], v158 offset:10240
	ds_read_b128 v[110:113], v160
	ds_read_b128 v[114:117], v160 offset:2048
	ds_read_b128 v[118:121], v160 offset:4096
	ds_read_b128 v[122:125], v160 offset:6144
	ds_read_b128 v[126:129], v160 offset:8192
	ds_read_b128 v[130:133], v160 offset:10240
	ds_read_b128 v[146:149], v164
	ds_read_b128 v[150:153], v164 offset:2048
	ds_read_b128 v[154:157], v164 offset:4096
	s_and_b64 vcc, exec, s[4:5]
	s_cbranch_vccnz .Lgemm_N_loop
	.p2align 3
	s_nop 0
.Lgemm_T_loop:
	s_waitcnt lgkmcnt(9)
	s_nop 0
	s_add_u32 m0, s11, 0x1e080
	v_mfma_f32_16x16x32_f16 v[82:85], v[134:137], v[86:89], v[82:85]
	global_load_lds_dwordx4 v[220:221], off offset:-128
	v_mfma_f32_16x16x32_f16 v[58:61], v[138:141], v[86:89], v[58:61]
	v_mfma_f32_16x16x32_f16 v[14:17], v[142:145], v[86:89], v[14:17]
	v_mfma_f32_16x16x32_f16 v[78:81], v[134:137], v[90:93], v[78:81]
	v_mfma_f32_16x16x32_f16 v[22:25], v[138:141], v[90:93], v[22:25]
	v_mfma_f32_16x16x32_f16 v[30:33], v[142:145], v[90:93], v[30:33]
	s_add_u32 m0, s11, 0x20080
	v_mfma_f32_16x16x32_f16 v[74:77], v[134:137], v[94:97], v[74:77]
	global_load_lds_dwordx4 v[224:225], off offset:-128
	v_mfma_f32_16x16x32_f16 v[18:21], v[138:141], v[94:97], v[18:21]
	v_mfma_f32_16x16x32_f16 v[26:29], v[142:145], v[94:97], v[26:29]
	v_mfma_f32_16x16x32_f16 v[70:73], v[134:137], v[98:101], v[70:73]
	v_mfma_f32_16x16x32_f16 v[46:49], v[138:141], v[98:101], v[46:49]
	v_mfma_f32_16x16x32_f16 v[240:243], v[142:145], v[98:101], v[240:243]
	s_add_u32 m0, s11, 0x22080
	v_mfma_f32_16x16x32_f16 v[66:69], v[134:137], v[102:105], v[66:69]
	global_load_lds_dwordx4 v[228:229], off offset:-128
	v_mfma_f32_16x16x32_f16 v[42:45], v[138:141], v[102:105], v[42:45]
	v_mfma_f32_16x16x32_f16 v[236:239], v[142:145], v[102:105], v[236:239]
	v_mfma_f32_16x16x32_f16 v[62:65], v[134:137], v[106:109], v[62:65]
	v_mfma_f32_16x16x32_f16 v[38:41], v[138:141], v[106:109], v[38:41]
	v_mfma_f32_16x16x32_f16 v[34:37], v[142:145], v[106:109], v[34:37]
	s_waitcnt vmcnt(6) lgkmcnt(0)
	s_barrier
	s_add_u32 m0, s11, 0x0
	s_nop 0
	ds_read_b128 v[134:137], v162 offset:49152
	global_load_lds_dwordx4 v[218:219], off
	v_mfma_f32_16x16x32_f16 v[82:85], v[146:149], v[110:113], v[82:85]
	ds_read_b128 v[138:141], v162 offset:51200
	v_mfma_f32_16x16x32_f16 v[58:61], v[150:153], v[110:113], v[58:61]
	ds_read_b128 v[142:145], v162 offset:53248
	v_mfma_f32_16x16x32_f16 v[14:17], v[154:157], v[110:113], v[14:17]
	ds_read_b128 v[86:89], v158 offset:49152
	v_mfma_f32_16x16x32_f16 v[78:81], v[146:149], v[114:117], v[78:81]
	ds_read_b128 v[90:93], v158 offset:51200
	v_mfma_f32_16x16x32_f16 v[22:25], v[150:153], v[114:117], v[22:25]
	ds_read_b128 v[94:97], v158 offset:53248
	v_mfma_f32_16x16x32_f16 v[30:33], v[154:157], v[114:117], v[30:33]
	s_add_u32 m0, s11, 0x2000
	ds_read_b128 v[98:101], v158 offset:55296
	global_load_lds_dwordx4 v[222:223], off
	v_mfma_f32_16x16x32_f16 v[74:77], v[146:149], v[118:121], v[74:77]
	ds_read_b128 v[102:105], v158 offset:57344
	v_mfma_f32_16x16x32_f16 v[18:21], v[150:153], v[118:121], v[18:21]
	ds_read_b128 v[106:109], v158 offset:59392
	v_mfma_f32_16x16x32_f16 v[26:29], v[154:157], v[118:121], v[26:29]
	ds_read_b128 v[110:113], v160 offset:49152
	v_mfma_f32_16x16x32_f16 v[70:73], v[146:149], v[122:125], v[70:73]
	ds_read_b128 v[114:117], v160 offset:51200
	v_mfma_f32_16x16x32_f16 v[46:49], v[150:153], v[122:125], v[46:49]
	v_mfma_f32_16x16x32_f16 v[240:243], v[154:157], v[122:125], v[240:243]
	s_add_u32 m0, s11, 0x4000
	ds_read_b128 v[118:121], v160 offset:53248
	global_load_lds_dwordx4 v[226:227], off
	v_mfma_f32_16x16x32_f16 v[66:69], v[146:149], v[126:129], v[66:69]
	ds_read_b128 v[122:125], v160 offset:55296
	v_mfma_f32_16x16x32_f16 v[42:45], v[150:153], v[126:129], v[42:45]
	v_mfma_f32_16x16x32_f16 v[236:239], v[154:157], v[126:129], v[236:239]
	ds_read_b128 v[126:129], v160 offset:57344
	v_mfma_f32_16x16x32_f16 v[62:65], v[146:149], v[130:133], v[62:65]
	v_mfma_f32_16x16x32_f16 v[38:41], v[150:153], v[130:133], v[38:41]
	v_mfma_f32_16x16x32_f16 v[34:37], v[154:157], v[130:133], v[34:37]
	ds_read_b128 v[130:133], v160 offset:59392
	ds_read_b128 v[146:149], v164 offset:49152
	ds_read_b128 v[150:153], v164 offset:51200
	ds_read_b128 v[154:157], v164 offset:53248
	s_waitcnt lgkmcnt(9)
	s_nop 0
	s_add_u32 m0, s11, 0x6000
	v_mfma_f32_16x16x32_f16 v[82:85], v[134:137], v[86:89], v[82:85]
	global_load_lds_dwordx4 v[220:221], off
	v_mfma_f32_16x16x32_f16 v[58:61], v[138:141], v[86:89], v[58:61]
	v_mfma_f32_16x16x32_f16 v[14:17], v[142:145], v[86:89], v[14:17]
	v_mfma_f32_16x16x32_f16 v[78:81], v[134:137], v[90:93], v[78:81]
	v_mfma_f32_16x16x32_f16 v[22:25], v[138:141], v[90:93], v[22:25]
	v_mfma_f32_16x16x32_f16 v[30:33], v[142:145], v[90:93], v[30:33]
	s_add_u32 m0, s11, 0x8000
	v_mfma_f32_16x16x32_f16 v[74:77], v[134:137], v[94:97], v[74:77]
	global_load_lds_dwordx4 v[224:225], off
	v_mfma_f32_16x16x32_f16 v[18:21], v[138:141], v[94:97], v[18:21]
	v_mfma_f32_16x16x32_f16 v[26:29], v[142:145], v[94:97], v[26:29]
	v_mfma_f32_16x16x32_f16 v[70:73], v[134:137], v[98:101], v[70:73]
	v_mfma_f32_16x16x32_f16 v[46:49], v[138:141], v[98:101], v[46:49]
	v_mfma_f32_16x16x32_f16 v[240:243], v[142:145], v[98:101], v[240:243]
	s_add_u32 m0, s11, 0xa000
	v_mfma_f32_16x16x32_f16 v[66:69], v[134:137], v[102:105], v[66:69]
	global_load_lds_dwordx4 v[228:229], off
	v_mfma_f32_16x16x32_f16 v[42:45], v[138:141], v[102:105], v[42:45]
	v_mfma_f32_16x16x32_f16 v[236:239], v[142:145], v[102:105], v[236:239]
	v_mfma_f32_16x16x32_f16 v[62:65], v[134:137], v[106:109], v[62:65]
	v_mfma_f32_16x16x32_f16 v[38:41], v[138:141], v[106:109], v[38:41]
	v_mfma_f32_16x16x32_f16 v[34:37], v[142:145], v[106:109], v[34:37]
	s_waitcnt vmcnt(6) lgkmcnt(0)
	s_barrier
	s_add_u32 m0, s11, 0xbf80
	ds_read_b128 v[134:137], v163
	global_load_lds_dwordx4 v[218:219], off offset:128
	v_mfma_f32_16x16x32_f16 v[82:85], v[146:149], v[110:113], v[82:85]
	ds_read_b128 v[138:141], v163 offset:2048
	v_mfma_f32_16x16x32_f16 v[58:61], v[150:153], v[110:113], v[58:61]
	ds_read_b128 v[142:145], v163 offset:4096
	v_mfma_f32_16x16x32_f16 v[14:17], v[154:157], v[110:113], v[14:17]
	ds_read_b128 v[86:89], v159
	v_mfma_f32_16x16x32_f16 v[78:81], v[146:149], v[114:117], v[78:81]
	ds_read_b128 v[90:93], v159 offset:2048
	v_mfma_f32_16x16x32_f16 v[22:25], v[150:153], v[114:117], v[22:25]
	ds_read_b128 v[94:97], v159 offset:4096
	v_mfma_f32_16x16x32_f16 v[30:33], v[154:157], v[114:117], v[30:33]
	s_add_u32 m0, s11, 0xdf80
	ds_read_b128 v[98:101], v159 offset:6144
	global_load_lds_dwordx4 v[222:223], off offset:128
	v_mfma_f32_16x16x32_f16 v[74:77], v[146:149], v[118:121], v[74:77]
	ds_read_b128 v[102:105], v159 offset:8192
	v_mfma_f32_16x16x32_f16 v[18:21], v[150:153], v[118:121], v[18:21]
	ds_read_b128 v[106:109], v159 offset:10240
	v_mfma_f32_16x16x32_f16 v[26:29], v[154:157], v[118:121], v[26:29]
	ds_read_b128 v[110:113], v161
	v_mfma_f32_16x16x32_f16 v[70:73], v[146:149], v[122:125], v[70:73]
	ds_read_b128 v[114:117], v161 offset:2048
	v_mfma_f32_16x16x32_f16 v[46:49], v[150:153], v[122:125], v[46:49]
	v_mfma_f32_16x16x32_f16 v[240:243], v[154:157], v[122:125], v[240:243]
	s_add_u32 m0, s11, 0xff80
	ds_read_b128 v[118:121], v161 offset:4096
	global_load_lds_dwordx4 v[226:227], off offset:128
	v_mfma_f32_16x16x32_f16 v[66:69], v[146:149], v[126:129], v[66:69]
	ds_read_b128 v[122:125], v161 offset:6144
	v_mfma_f32_16x16x32_f16 v[42:45], v[150:153], v[126:129], v[42:45]
	v_mfma_f32_16x16x32_f16 v[236:239], v[154:157], v[126:129], v[236:239]
	ds_read_b128 v[126:129], v161 offset:8192
	v_mfma_f32_16x16x32_f16 v[62:65], v[146:149], v[130:133], v[62:65]
	v_mfma_f32_16x16x32_f16 v[38:41], v[150:153], v[130:133], v[38:41]
	v_mfma_f32_16x16x32_f16 v[34:37], v[154:157], v[130:133], v[34:37]
	ds_read_b128 v[130:133], v161 offset:10240
	ds_read_b128 v[146:149], v165
	ds_read_b128 v[150:153], v165 offset:2048
	ds_read_b128 v[154:157], v165 offset:4096
	s_waitcnt lgkmcnt(9)
	s_nop 0
	s_add_u32 m0, s11, 0x11f80
	v_mfma_f32_16x16x32_f16 v[82:85], v[134:137], v[86:89], v[82:85]
	global_load_lds_dwordx4 v[220:221], off offset:128
	v_mfma_f32_16x16x32_f16 v[58:61], v[138:141], v[86:89], v[58:61]
	v_mfma_f32_16x16x32_f16 v[14:17], v[142:145], v[86:89], v[14:17]
	v_mfma_f32_16x16x32_f16 v[78:81], v[134:137], v[90:93], v[78:81]
	v_mfma_f32_16x16x32_f16 v[22:25], v[138:141], v[90:93], v[22:25]
	v_mfma_f32_16x16x32_f16 v[30:33], v[142:145], v[90:93], v[30:33]
	s_add_u32 m0, s11, 0x13f80
	v_mfma_f32_16x16x32_f16 v[74:77], v[134:137], v[94:97], v[74:77]
	global_load_lds_dwordx4 v[224:225], off offset:128
	v_mfma_f32_16x16x32_f16 v[18:21], v[138:141], v[94:97], v[18:21]
	v_mfma_f32_16x16x32_f16 v[26:29], v[142:145], v[94:97], v[26:29]
	v_mfma_f32_16x16x32_f16 v[70:73], v[134:137], v[98:101], v[70:73]
	v_mfma_f32_16x16x32_f16 v[46:49], v[138:141], v[98:101], v[46:49]
	v_mfma_f32_16x16x32_f16 v[240:243], v[142:145], v[98:101], v[240:243]
	s_add_u32 m0, s11, 0x15f80
	v_mfma_f32_16x16x32_f16 v[66:69], v[134:137], v[102:105], v[66:69]
	global_load_lds_dwordx4 v[228:229], off offset:128
	v_mfma_f32_16x16x32_f16 v[42:45], v[138:141], v[102:105], v[42:45]
	v_mfma_f32_16x16x32_f16 v[236:239], v[142:145], v[102:105], v[236:239]
	v_mfma_f32_16x16x32_f16 v[62:65], v[134:137], v[106:109], v[62:65]
	v_mfma_f32_16x16x32_f16 v[38:41], v[138:141], v[106:109], v[38:41]
	v_mfma_f32_16x16x32_f16 v[34:37], v[142:145], v[106:109], v[34:37]
	s_waitcnt vmcnt(6) lgkmcnt(0)
	s_barrier
	s_add_u32 m0, s11, 0x17f00
	ds_read_b128 v[134:137], v162
	global_load_lds_dwordx4 v[218:219], off offset:256
	v_mfma_f32_16x16x32_f16 v[82:85], v[146:149], v[110:113], v[82:85]
	ds_read_b128 v[138:141], v162 offset:2048
	v_mfma_f32_16x16x32_f16 v[58:61], v[150:153], v[110:113], v[58:61]
	ds_read_b128 v[142:145], v162 offset:4096
	v_mfma_f32_16x16x32_f16 v[14:17], v[154:157], v[110:113], v[14:17]
	ds_read_b128 v[86:89], v158
	v_mfma_f32_16x16x32_f16 v[78:81], v[146:149], v[114:117], v[78:81]
	ds_read_b128 v[90:93], v158 offset:2048
	v_mfma_f32_16x16x32_f16 v[22:25], v[150:153], v[114:117], v[22:25]
	ds_read_b128 v[94:97], v158 offset:4096
	v_mfma_f32_16x16x32_f16 v[30:33], v[154:157], v[114:117], v[30:33]
	s_add_u32 m0, s11, 0x19f00
	ds_read_b128 v[98:101], v158 offset:6144
	global_load_lds_dwordx4 v[222:223], off offset:256
	v_mfma_f32_16x16x32_f16 v[74:77], v[146:149], v[118:121], v[74:77]
	ds_read_b128 v[102:105], v158 offset:8192
	v_mfma_f32_16x16x32_f16 v[18:21], v[150:153], v[118:121], v[18:21]
	ds_read_b128 v[106:109], v158 offset:10240
	v_mfma_f32_16x16x32_f16 v[26:29], v[154:157], v[118:121], v[26:29]
	ds_read_b128 v[110:113], v160
	v_mfma_f32_16x16x32_f16 v[70:73], v[146:149], v[122:125], v[70:73]
	ds_read_b128 v[114:117], v160 offset:2048
	v_mfma_f32_16x16x32_f16 v[46:49], v[150:153], v[122:125], v[46:49]
	v_mfma_f32_16x16x32_f16 v[240:243], v[154:157], v[122:125], v[240:243]
	s_add_u32 m0, s11, 0x1bf00
	ds_read_b128 v[118:121], v160 offset:4096
	global_load_lds_dwordx4 v[226:227], off offset:256
	v_mfma_f32_16x16x32_f16 v[66:69], v[146:149], v[126:129], v[66:69]
	ds_read_b128 v[122:125], v160 offset:6144
	v_mfma_f32_16x16x32_f16 v[42:45], v[150:153], v[126:129], v[42:45]
	v_mfma_f32_16x16x32_f16 v[236:239], v[154:157], v[126:129], v[236:239]
	ds_read_b128 v[126:129], v160 offset:8192
	v_mfma_f32_16x16x32_f16 v[62:65], v[146:149], v[130:133], v[62:65]
	v_mfma_f32_16x16x32_f16 v[38:41], v[150:153], v[130:133], v[38:41]
	v_mfma_f32_16x16x32_f16 v[34:37], v[154:157], v[130:133], v[34:37]
	ds_read_b128 v[130:133], v160 offset:10240
	ds_read_b128 v[146:149], v164
	ds_read_b128 v[150:153], v164 offset:2048
	ds_read_b128 v[154:157], v164 offset:4096
	v_lshl_add_u64 v[218:219], v[218:219], 0, s[20:21]
	v_lshl_add_u64 v[222:223], v[222:223], 0, s[20:21]
	v_lshl_add_u64 v[226:227], v[226:227], 0, s[20:21]
	v_lshl_add_u64 v[220:221], v[220:221], 0, s[20:21]
	v_lshl_add_u64 v[224:225], v[224:225], 0, s[20:21]
	v_lshl_add_u64 v[228:229], v[228:229], 0, s[20:21]
	s_nop 0
	s_sub_u32 s22, s22, 1
	s_cmp_lg_u32 s22, 0
	s_cbranch_scc1 .Lgemm_T_loop
	s_waitcnt lgkmcnt(9)
	s_nop 0
	s_add_u32 m0, s11, 0x1e080
	v_mfma_f32_16x16x32_f16 v[82:85], v[134:137], v[86:89], v[82:85]
	global_load_lds_dwordx4 v[220:221], off offset:-128
	v_mfma_f32_16x16x32_f16 v[58:61], v[138:141], v[86:89], v[58:61]
	v_mfma_f32_16x16x32_f16 v[14:17], v[142:145], v[86:89], v[14:17]
	v_mfma_f32_16x16x32_f16 v[78:81], v[134:137], v[90:93], v[78:81]
	v_mfma_f32_16x16x32_f16 v[22:25], v[138:141], v[90:93], v[22:25]
	v_mfma_f32_16x16x32_f16 v[30:33], v[142:145], v[90:93], v[30:33]
	s_add_u32 m0, s11, 0x20080
	v_mfma_f32_16x16x32_f16 v[74:77], v[134:137], v[94:97], v[74:77]
	global_load_lds_dwordx4 v[224:225], off offset:-128
	v_mfma_f32_16x16x32_f16 v[18:21], v[138:141], v[94:97], v[18:21]
	v_mfma_f32_16x16x32_f16 v[26:29], v[142:145], v[94:97], v[26:29]
	v_mfma_f32_16x16x32_f16 v[70:73], v[134:137], v[98:101], v[70:73]
	v_mfma_f32_16x16x32_f16 v[46:49], v[138:141], v[98:101], v[46:49]
	v_mfma_f32_16x16x32_f16 v[240:243], v[142:145], v[98:101], v[240:243]
	s_add_u32 m0, s11, 0x22080
	v_mfma_f32_16x16x32_f16 v[66:69], v[134:137], v[102:105], v[66:69]
	global_load_lds_dwordx4 v[228:229], off offset:-128
	v_mfma_f32_16x16x32_f16 v[42:45], v[138:141], v[102:105], v[42:45]
	v_mfma_f32_16x16x32_f16 v[236:239], v[142:145], v[102:105], v[236:239]
	v_mfma_f32_16x16x32_f16 v[62:65], v[134:137], v[106:109], v[62:65]
	v_mfma_f32_16x16x32_f16 v[38:41], v[138:141], v[106:109], v[38:41]
	v_mfma_f32_16x16x32_f16 v[34:37], v[142:145], v[106:109], v[34:37]
	s_waitcnt vmcnt(6) lgkmcnt(0)
	s_barrier
	s_add_u32 m0, s11, 0x0
	s_nop 0
	ds_read_b128 v[134:137], v162 offset:49152
	global_load_lds_dwordx4 v[218:219], off
	v_mfma_f32_16x16x32_f16 v[82:85], v[146:149], v[110:113], v[82:85]
	ds_read_b128 v[138:141], v162 offset:51200
	v_mfma_f32_16x16x32_f16 v[58:61], v[150:153], v[110:113], v[58:61]
	ds_read_b128 v[142:145], v162 offset:53248
	v_mfma_f32_16x16x32_f16 v[14:17], v[154:157], v[110:113], v[14:17]
	ds_read_b128 v[86:89], v158 offset:49152
	v_mfma_f32_16x16x32_f16 v[78:81], v[146:149], v[114:117], v[78:81]
	ds_read_b128 v[90:93], v158 offset:51200
	v_mfma_f32_16x16x32_f16 v[22:25], v[150:153], v[114:117], v[22:25]
	ds_read_b128 v[94:97], v158 offset:53248
	v_mfma_f32_16x16x32_f16 v[30:33], v[154:157], v[114:117], v[30:33]
	s_add_u32 m0, s11, 0x2000
	ds_read_b128 v[98:101], v158 offset:55296
	global_load_lds_dwordx4 v[222:223], off
	v_mfma_f32_16x16x32_f16 v[74:77], v[146:149], v[118:121], v[74:77]
	ds_read_b128 v[102:105], v158 offset:57344
	v_mfma_f32_16x16x32_f16 v[18:21], v[150:153], v[118:121], v[18:21]
	ds_read_b128 v[106:109], v158 offset:59392
	v_mfma_f32_16x16x32_f16 v[26:29], v[154:157], v[118:121], v[26:29]
	ds_read_b128 v[110:113], v160 offset:49152
	v_mfma_f32_16x16x32_f16 v[70:73], v[146:149], v[122:125], v[70:73]
	ds_read_b128 v[114:117], v160 offset:51200
	v_mfma_f32_16x16x32_f16 v[46:49], v[150:153], v[122:125], v[46:49]
	v_mfma_f32_16x16x32_f16 v[240:243], v[154:157], v[122:125], v[240:243]
	s_add_u32 m0, s11, 0x4000
	ds_read_b128 v[118:121], v160 offset:53248
	global_load_lds_dwordx4 v[226:227], off
	v_mfma_f32_16x16x32_f16 v[66:69], v[146:149], v[126:129], v[66:69]
	ds_read_b128 v[122:125], v160 offset:55296
	v_mfma_f32_16x16x32_f16 v[42:45], v[150:153], v[126:129], v[42:45]
	v_mfma_f32_16x16x32_f16 v[236:239], v[154:157], v[126:129], v[236:239]
	ds_read_b128 v[126:129], v160 offset:57344
	v_mfma_f32_16x16x32_f16 v[62:65], v[146:149], v[130:133], v[62:65]
	v_mfma_f32_16x16x32_f16 v[38:41], v[150:153], v[130:133], v[38:41]
	v_mfma_f32_16x16x32_f16 v[34:37], v[154:157], v[130:133], v[34:37]
	ds_read_b128 v[130:133], v160 offset:59392
	ds_read_b128 v[146:149], v164 offset:49152
	ds_read_b128 v[150:153], v164 offset:51200
	ds_read_b128 v[154:157], v164 offset:53248
	s_waitcnt lgkmcnt(9)
	s_nop 0
	s_add_u32 m0, s11, 0x6000
	v_mfma_f32_16x16x32_f16 v[82:85], v[134:137], v[86:89], v[82:85]
	global_load_lds_dwordx4 v[220:221], off
	v_mfma_f32_16x16x32_f16 v[58:61], v[138:141], v[86:89], v[58:61]
	v_mfma_f32_16x16x32_f16 v[14:17], v[142:145], v[86:89], v[14:17]
	v_mfma_f32_16x16x32_f16 v[78:81], v[134:137], v[90:93], v[78:81]
	v_mfma_f32_16x16x32_f16 v[22:25], v[138:141], v[90:93], v[22:25]
	v_mfma_f32_16x16x32_f16 v[30:33], v[142:145], v[90:93], v[30:33]
	s_add_u32 m0, s11, 0x8000
	v_mfma_f32_16x16x32_f16 v[74:77], v[134:137], v[94:97], v[74:77]
	global_load_lds_dwordx4 v[224:225], off
	v_mfma_f32_16x16x32_f16 v[18:21], v[138:141], v[94:97], v[18:21]
	v_mfma_f32_16x16x32_f16 v[26:29], v[142:145], v[94:97], v[26:29]
	v_mfma_f32_16x16x32_f16 v[70:73], v[134:137], v[98:101], v[70:73]
	v_mfma_f32_16x16x32_f16 v[46:49], v[138:141], v[98:101], v[46:49]
	v_mfma_f32_16x16x32_f16 v[240:243], v[142:145], v[98:101], v[240:243]
	s_add_u32 m0, s11, 0xa000
	v_mfma_f32_16x16x32_f16 v[66:69], v[134:137], v[102:105], v[66:69]
	global_load_lds_dwordx4 v[228:229], off
	v_mfma_f32_16x16x32_f16 v[42:45], v[138:141], v[102:105], v[42:45]
	v_mfma_f32_16x16x32_f16 v[236:239], v[142:145], v[102:105], v[236:239]
	v_mfma_f32_16x16x32_f16 v[62:65], v[134:137], v[106:109], v[62:65]
	v_mfma_f32_16x16x32_f16 v[38:41], v[138:141], v[106:109], v[38:41]
	v_mfma_f32_16x16x32_f16 v[34:37], v[142:145], v[106:109], v[34:37]
	s_waitcnt vmcnt(6) lgkmcnt(0)
	s_barrier
	s_lshl_b32 s26, s17, 2
	s_add_u32 s26, s24, s26
	s_addc_u32 s27, s25, 0
	v_lshlrev_b32_e32 v50, 4, v231
	global_load_dwordx4 v[10:13], v50, s[26:27]
	global_load_dwordx4 v[6:9], v50, s[26:27] offset:64
	global_load_dwordx4 v[2:5], v50, s[26:27] offset:128
	ds_read_b128 v[134:137], v163
	v_mfma_f32_16x16x32_f16 v[82:85], v[146:149], v[110:113], v[82:85]
	ds_read_b128 v[138:141], v163 offset:2048
	v_mfma_f32_16x16x32_f16 v[58:61], v[150:153], v[110:113], v[58:61]
	ds_read_b128 v[142:145], v163 offset:4096
	v_mfma_f32_16x16x32_f16 v[14:17], v[154:157], v[110:113], v[14:17]
	ds_read_b128 v[86:89], v159
	v_mfma_f32_16x16x32_f16 v[78:81], v[146:149], v[114:117], v[78:81]
	ds_read_b128 v[90:93], v159 offset:2048
	v_mfma_f32_16x16x32_f16 v[22:25], v[150:153], v[114:117], v[22:25]
	ds_read_b128 v[94:97], v159 offset:4096
	v_mfma_f32_16x16x32_f16 v[30:33], v[154:157], v[114:117], v[30:33]
	ds_read_b128 v[98:101], v159 offset:6144
	v_mfma_f32_16x16x32_f16 v[74:77], v[146:149], v[118:121], v[74:77]
	ds_read_b128 v[102:105], v159 offset:8192
	v_mfma_f32_16x16x32_f16 v[18:21], v[150:153], v[118:121], v[18:21]
	ds_read_b128 v[106:109], v159 offset:10240
	v_mfma_f32_16x16x32_f16 v[26:29], v[154:157], v[118:121], v[26:29]
	ds_read_b128 v[110:113], v161
	v_mfma_f32_16x16x32_f16 v[70:73], v[146:149], v[122:125], v[70:73]
	ds_read_b128 v[114:117], v161 offset:2048
	v_mfma_f32_16x16x32_f16 v[46:49], v[150:153], v[122:125], v[46:49]
	v_mfma_f32_16x16x32_f16 v[240:243], v[154:157], v[122:125], v[240:243]
	ds_read_b128 v[118:121], v161 offset:4096
	v_mfma_f32_16x16x32_f16 v[66:69], v[146:149], v[126:129], v[66:69]
	ds_read_b128 v[122:125], v161 offset:6144
	v_mfma_f32_16x16x32_f16 v[42:45], v[150:153], v[126:129], v[42:45]
	v_mfma_f32_16x16x32_f16 v[236:239], v[154:157], v[126:129], v[236:239]
	ds_read_b128 v[126:129], v161 offset:8192
	v_mfma_f32_16x16x32_f16 v[62:65], v[146:149], v[130:133], v[62:65]
	v_mfma_f32_16x16x32_f16 v[38:41], v[150:153], v[130:133], v[38:41]
	v_mfma_f32_16x16x32_f16 v[34:37], v[154:157], v[130:133], v[34:37]
	ds_read_b128 v[130:133], v161 offset:10240
	ds_read_b128 v[146:149], v165
	ds_read_b128 v[150:153], v165 offset:2048
	ds_read_b128 v[154:157], v165 offset:4096
	s_waitcnt lgkmcnt(9)
	s_nop 0
	v_mfma_f32_16x16x32_f16 v[82:85], v[134:137], v[86:89], v[82:85]
	v_mfma_f32_16x16x32_f16 v[58:61], v[138:141], v[86:89], v[58:61]
	v_mfma_f32_16x16x32_f16 v[14:17], v[142:145], v[86:89], v[14:17]
	v_mfma_f32_16x16x32_f16 v[78:81], v[134:137], v[90:93], v[78:81]
	v_mfma_f32_16x16x32_f16 v[22:25], v[138:141], v[90:93], v[22:25]
	v_mfma_f32_16x16x32_f16 v[30:33], v[142:145], v[90:93], v[30:33]
	v_mfma_f32_16x16x32_f16 v[74:77], v[134:137], v[94:97], v[74:77]
	v_mfma_f32_16x16x32_f16 v[18:21], v[138:141], v[94:97], v[18:21]
	v_mfma_f32_16x16x32_f16 v[26:29], v[142:145], v[94:97], v[26:29]
	v_mfma_f32_16x16x32_f16 v[70:73], v[134:137], v[98:101], v[70:73]
	v_mfma_f32_16x16x32_f16 v[46:49], v[138:141], v[98:101], v[46:49]
	v_mfma_f32_16x16x32_f16 v[240:243], v[142:145], v[98:101], v[240:243]
	v_mfma_f32_16x16x32_f16 v[66:69], v[134:137], v[102:105], v[66:69]
	v_mfma_f32_16x16x32_f16 v[42:45], v[138:141], v[102:105], v[42:45]
	v_mfma_f32_16x16x32_f16 v[236:239], v[142:145], v[102:105], v[236:239]
	v_mfma_f32_16x16x32_f16 v[62:65], v[134:137], v[106:109], v[62:65]
	v_mfma_f32_16x16x32_f16 v[38:41], v[138:141], v[106:109], v[38:41]
	v_mfma_f32_16x16x32_f16 v[34:37], v[142:145], v[106:109], v[34:37]
	s_waitcnt vmcnt(3) lgkmcnt(0)
	s_barrier
	ds_read_b128 v[134:137], v162
	v_mfma_f32_16x16x32_f16 v[82:85], v[146:149], v[110:113], v[82:85]
	ds_read_b128 v[138:141], v162 offset:2048
	v_mfma_f32_16x16x32_f16 v[58:61], v[150:153], v[110:113], v[58:61]
	ds_read_b128 v[142:145], v162 offset:4096
	v_mfma_f32_16x16x32_f16 v[14:17], v[154:157], v[110:113], v[14:17]
	ds_read_b128 v[86:89], v158
	v_mfma_f32_16x16x32_f16 v[78:81], v[146:149], v[114:117], v[78:81]
	ds_read_b128 v[90:93], v158 offset:2048
	v_mfma_f32_16x16x32_f16 v[22:25], v[150:153], v[114:117], v[22:25]
	ds_read_b128 v[94:97], v158 offset:4096
	v_mfma_f32_16x16x32_f16 v[30:33], v[154:157], v[114:117], v[30:33]
	ds_read_b128 v[98:101], v158 offset:6144
	v_mfma_f32_16x16x32_f16 v[74:77], v[146:149], v[118:121], v[74:77]
	ds_read_b128 v[102:105], v158 offset:8192
	v_mfma_f32_16x16x32_f16 v[18:21], v[150:153], v[118:121], v[18:21]
	ds_read_b128 v[106:109], v158 offset:10240
	v_mfma_f32_16x16x32_f16 v[26:29], v[154:157], v[118:121], v[26:29]
	ds_read_b128 v[110:113], v160
	v_mfma_f32_16x16x32_f16 v[70:73], v[146:149], v[122:125], v[70:73]
	ds_read_b128 v[114:117], v160 offset:2048
	v_mfma_f32_16x16x32_f16 v[46:49], v[150:153], v[122:125], v[46:49]
	v_mfma_f32_16x16x32_f16 v[240:243], v[154:157], v[122:125], v[240:243]
	ds_read_b128 v[118:121], v160 offset:4096
	v_mfma_f32_16x16x32_f16 v[66:69], v[146:149], v[126:129], v[66:69]
	ds_read_b128 v[122:125], v160 offset:6144
	v_mfma_f32_16x16x32_f16 v[42:45], v[150:153], v[126:129], v[42:45]
	v_mfma_f32_16x16x32_f16 v[236:239], v[154:157], v[126:129], v[236:239]
	ds_read_b128 v[126:129], v160 offset:8192
	v_mfma_f32_16x16x32_f16 v[62:65], v[146:149], v[130:133], v[62:65]
	v_mfma_f32_16x16x32_f16 v[38:41], v[150:153], v[130:133], v[38:41]
	v_mfma_f32_16x16x32_f16 v[34:37], v[154:157], v[130:133], v[34:37]
	ds_read_b128 v[130:133], v160 offset:10240
	ds_read_b128 v[146:149], v164
	ds_read_b128 v[150:153], v164 offset:2048
	ds_read_b128 v[154:157], v164 offset:4096
	s_waitcnt lgkmcnt(9)
	s_nop 0
	v_mfma_f32_16x16x32_f16 v[82:85], v[134:137], v[86:89], v[82:85]
	v_mfma_f32_16x16x32_f16 v[58:61], v[138:141], v[86:89], v[58:61]
	v_mfma_f32_16x16x32_f16 v[14:17], v[142:145], v[86:89], v[14:17]
	v_mfma_f32_16x16x32_f16 v[78:81], v[134:137], v[90:93], v[78:81]
	v_mfma_f32_16x16x32_f16 v[22:25], v[138:141], v[90:93], v[22:25]
	v_mfma_f32_16x16x32_f16 v[30:33], v[142:145], v[90:93], v[30:33]
	v_mfma_f32_16x16x32_f16 v[74:77], v[134:137], v[94:97], v[74:77]
	v_mfma_f32_16x16x32_f16 v[18:21], v[138:141], v[94:97], v[18:21]
	v_mfma_f32_16x16x32_f16 v[26:29], v[142:145], v[94:97], v[26:29]
	v_mfma_f32_16x16x32_f16 v[70:73], v[134:137], v[98:101], v[70:73]
	v_mfma_f32_16x16x32_f16 v[46:49], v[138:141], v[98:101], v[46:49]
	v_mfma_f32_16x16x32_f16 v[240:243], v[142:145], v[98:101], v[240:243]
	v_mfma_f32_16x16x32_f16 v[66:69], v[134:137], v[102:105], v[66:69]
	v_mfma_f32_16x16x32_f16 v[42:45], v[138:141], v[102:105], v[42:45]
	v_mfma_f32_16x16x32_f16 v[236:239], v[142:145], v[102:105], v[236:239]
	v_mfma_f32_16x16x32_f16 v[62:65], v[134:137], v[106:109], v[62:65]
	v_mfma_f32_16x16x32_f16 v[38:41], v[138:141], v[106:109], v[38:41]
	v_mfma_f32_16x16x32_f16 v[34:37], v[142:145], v[106:109], v[34:37]
	s_waitcnt lgkmcnt(0)
	v_mfma_f32_16x16x32_f16 v[82:85], v[146:149], v[110:113], v[82:85]
	v_mfma_f32_16x16x32_f16 v[58:61], v[150:153], v[110:113], v[58:61]
	v_mfma_f32_16x16x32_f16 v[14:17], v[154:157], v[110:113], v[14:17]
	v_mfma_f32_16x16x32_f16 v[78:81], v[146:149], v[114:117], v[78:81]
	v_mfma_f32_16x16x32_f16 v[22:25], v[150:153], v[114:117], v[22:25]
	v_mfma_f32_16x16x32_f16 v[30:33], v[154:157], v[114:117], v[30:33]
	v_mfma_f32_16x16x32_f16 v[74:77], v[146:149], v[118:121], v[74:77]
	v_mfma_f32_16x16x32_f16 v[18:21], v[150:153], v[118:121], v[18:21]
	v_mfma_f32_16x16x32_f16 v[26:29], v[154:157], v[118:121], v[26:29]
	v_mfma_f32_16x16x32_f16 v[70:73], v[146:149], v[122:125], v[70:73]
	v_mfma_f32_16x16x32_f16 v[46:49], v[150:153], v[122:125], v[46:49]
	v_mfma_f32_16x16x32_f16 v[240:243], v[154:157], v[122:125], v[240:243]
	v_mfma_f32_16x16x32_f16 v[66:69], v[146:149], v[126:129], v[66:69]
	v_mfma_f32_16x16x32_f16 v[42:45], v[150:153], v[126:129], v[42:45]
	v_mfma_f32_16x16x32_f16 v[236:239], v[154:157], v[126:129], v[236:239]
	v_mfma_f32_16x16x32_f16 v[62:65], v[146:149], v[130:133], v[62:65]
	v_mfma_f32_16x16x32_f16 v[38:41], v[150:153], v[130:133], v[38:41]
	v_mfma_f32_16x16x32_f16 v[34:37], v[154:157], v[130:133], v[34:37]
	s_branch .LBB1_76
	.p2align 3
	s_nop 0
.Lgemm_N_loop:
	s_waitcnt lgkmcnt(9)
	s_nop 0
	s_add_u32 m0, s11, 0x1e080
	v_mfma_f32_16x16x32_f16 v[82:85], v[86:89], v[134:137], v[82:85]
	global_load_lds_dwordx4 v[220:221], off offset:-128
	v_mfma_f32_16x16x32_f16 v[58:61], v[86:89], v[138:141], v[58:61]
	v_mfma_f32_16x16x32_f16 v[14:17], v[86:89], v[142:145], v[14:17]
	v_mfma_f32_16x16x32_f16 v[78:81], v[90:93], v[134:137], v[78:81]
	v_mfma_f32_16x16x32_f16 v[22:25], v[90:93], v[138:141], v[22:25]
	v_mfma_f32_16x16x32_f16 v[30:33], v[90:93], v[142:145], v[30:33]
	s_add_u32 m0, s11, 0x20080
	v_mfma_f32_16x16x32_f16 v[74:77], v[94:97], v[134:137], v[74:77]
	global_load_lds_dwordx4 v[224:225], off offset:-128
	v_mfma_f32_16x16x32_f16 v[18:21], v[94:97], v[138:141], v[18:21]
	v_mfma_f32_16x16x32_f16 v[26:29], v[94:97], v[142:145], v[26:29]
	v_mfma_f32_16x16x32_f16 v[70:73], v[98:101], v[134:137], v[70:73]
	v_mfma_f32_16x16x32_f16 v[46:49], v[98:101], v[138:141], v[46:49]
	v_mfma_f32_16x16x32_f16 v[240:243], v[98:101], v[142:145], v[240:243]
	s_add_u32 m0, s11, 0x22080
	v_mfma_f32_16x16x32_f16 v[66:69], v[102:105], v[134:137], v[66:69]
	global_load_lds_dwordx4 v[228:229], off offset:-128
	v_mfma_f32_16x16x32_f16 v[42:45], v[102:105], v[138:141], v[42:45]
	v_mfma_f32_16x16x32_f16 v[236:239], v[102:105], v[142:145], v[236:239]
	v_mfma_f32_16x16x32_f16 v[62:65], v[106:109], v[134:137], v[62:65]
	v_mfma_f32_16x16x32_f16 v[38:41], v[106:109], v[138:141], v[38:41]
	v_mfma_f32_16x16x32_f16 v[34:37], v[106:109], v[142:145], v[34:37]
	s_waitcnt vmcnt(6) lgkmcnt(0)
	s_barrier
	s_add_u32 m0, s11, 0x0
	s_nop 0
	ds_read_b128 v[134:137], v162 offset:49152
	global_load_lds_dwordx4 v[218:219], off
	v_mfma_f32_16x16x32_f16 v[82:85], v[110:113], v[146:149], v[82:85]
	ds_read_b128 v[138:141], v162 offset:51200
	v_mfma_f32_16x16x32_f16 v[58:61], v[110:113], v[150:153], v[58:61]
	ds_read_b128 v[142:145], v162 offset:53248
	v_mfma_f32_16x16x32_f16 v[14:17], v[110:113], v[154:157], v[14:17]
	ds_read_b128 v[86:89], v158 offset:49152
	v_mfma_f32_16x16x32_f16 v[78:81], v[114:117], v[146:149], v[78:81]
	ds_read_b128 v[90:93], v158 offset:51200
	v_mfma_f32_16x16x32_f16 v[22:25], v[114:117], v[150:153], v[22:25]
	ds_read_b128 v[94:97], v158 offset:53248
	v_mfma_f32_16x16x32_f16 v[30:33], v[114:117], v[154:157], v[30:33]
	s_add_u32 m0, s11, 0x2000
	ds_read_b128 v[98:101], v158 offset:55296
	global_load_lds_dwordx4 v[222:223], off
	v_mfma_f32_16x16x32_f16 v[74:77], v[118:121], v[146:149], v[74:77]
	ds_read_b128 v[102:105], v158 offset:57344
	v_mfma_f32_16x16x32_f16 v[18:21], v[118:121], v[150:153], v[18:21]
	ds_read_b128 v[106:109], v158 offset:59392
	v_mfma_f32_16x16x32_f16 v[26:29], v[118:121], v[154:157], v[26:29]
	ds_read_b128 v[110:113], v160 offset:49152
	v_mfma_f32_16x16x32_f16 v[70:73], v[122:125], v[146:149], v[70:73]
	ds_read_b128 v[114:117], v160 offset:51200
	v_mfma_f32_16x16x32_f16 v[46:49], v[122:125], v[150:153], v[46:49]
	v_mfma_f32_16x16x32_f16 v[240:243], v[122:125], v[154:157], v[240:243]
	s_add_u32 m0, s11, 0x4000
	ds_read_b128 v[118:121], v160 offset:53248
	global_load_lds_dwordx4 v[226:227], off
	v_mfma_f32_16x16x32_f16 v[66:69], v[126:129], v[146:149], v[66:69]
	ds_read_b128 v[122:125], v160 offset:55296
	v_mfma_f32_16x16x32_f16 v[42:45], v[126:129], v[150:153], v[42:45]
	v_mfma_f32_16x16x32_f16 v[236:239], v[126:129], v[154:157], v[236:239]
	ds_read_b128 v[126:129], v160 offset:57344
	v_mfma_f32_16x16x32_f16 v[62:65], v[130:133], v[146:149], v[62:65]
	v_mfma_f32_16x16x32_f16 v[38:41], v[130:133], v[150:153], v[38:41]
	v_mfma_f32_16x16x32_f16 v[34:37], v[130:133], v[154:157], v[34:37]
	ds_read_b128 v[130:133], v160 offset:59392
	ds_read_b128 v[146:149], v164 offset:49152
	ds_read_b128 v[150:153], v164 offset:51200
	ds_read_b128 v[154:157], v164 offset:53248
	s_waitcnt lgkmcnt(9)
	s_nop 0
	s_add_u32 m0, s11, 0x6000
	v_mfma_f32_16x16x32_f16 v[82:85], v[86:89], v[134:137], v[82:85]
	global_load_lds_dwordx4 v[220:221], off
	v_mfma_f32_16x16x32_f16 v[58:61], v[86:89], v[138:141], v[58:61]
	v_mfma_f32_16x16x32_f16 v[14:17], v[86:89], v[142:145], v[14:17]
	v_mfma_f32_16x16x32_f16 v[78:81], v[90:93], v[134:137], v[78:81]
	v_mfma_f32_16x16x32_f16 v[22:25], v[90:93], v[138:141], v[22:25]
	v_mfma_f32_16x16x32_f16 v[30:33], v[90:93], v[142:145], v[30:33]
	s_add_u32 m0, s11, 0x8000
	v_mfma_f32_16x16x32_f16 v[74:77], v[94:97], v[134:137], v[74:77]
	global_load_lds_dwordx4 v[224:225], off
	v_mfma_f32_16x16x32_f16 v[18:21], v[94:97], v[138:141], v[18:21]
	v_mfma_f32_16x16x32_f16 v[26:29], v[94:97], v[142:145], v[26:29]
	v_mfma_f32_16x16x32_f16 v[70:73], v[98:101], v[134:137], v[70:73]
	v_mfma_f32_16x16x32_f16 v[46:49], v[98:101], v[138:141], v[46:49]
	v_mfma_f32_16x16x32_f16 v[240:243], v[98:101], v[142:145], v[240:243]
	s_add_u32 m0, s11, 0xa000
	v_mfma_f32_16x16x32_f16 v[66:69], v[102:105], v[134:137], v[66:69]
	global_load_lds_dwordx4 v[228:229], off
	v_mfma_f32_16x16x32_f16 v[42:45], v[102:105], v[138:141], v[42:45]
	v_mfma_f32_16x16x32_f16 v[236:239], v[102:105], v[142:145], v[236:239]
	v_mfma_f32_16x16x32_f16 v[62:65], v[106:109], v[134:137], v[62:65]
	v_mfma_f32_16x16x32_f16 v[38:41], v[106:109], v[138:141], v[38:41]
	v_mfma_f32_16x16x32_f16 v[34:37], v[106:109], v[142:145], v[34:37]
	s_waitcnt vmcnt(6) lgkmcnt(0)
	s_barrier
	s_add_u32 m0, s11, 0xbf80
	ds_read_b128 v[134:137], v163
	global_load_lds_dwordx4 v[218:219], off offset:128
	v_mfma_f32_16x16x32_f16 v[82:85], v[110:113], v[146:149], v[82:85]
	ds_read_b128 v[138:141], v163 offset:2048
	v_mfma_f32_16x16x32_f16 v[58:61], v[110:113], v[150:153], v[58:61]
	ds_read_b128 v[142:145], v163 offset:4096
	v_mfma_f32_16x16x32_f16 v[14:17], v[110:113], v[154:157], v[14:17]
	ds_read_b128 v[86:89], v159
	v_mfma_f32_16x16x32_f16 v[78:81], v[114:117], v[146:149], v[78:81]
	ds_read_b128 v[90:93], v159 offset:2048
	v_mfma_f32_16x16x32_f16 v[22:25], v[114:117], v[150:153], v[22:25]
	ds_read_b128 v[94:97], v159 offset:4096
	v_mfma_f32_16x16x32_f16 v[30:33], v[114:117], v[154:157], v[30:33]
	s_add_u32 m0, s11, 0xdf80
	ds_read_b128 v[98:101], v159 offset:6144
	global_load_lds_dwordx4 v[222:223], off offset:128
	v_mfma_f32_16x16x32_f16 v[74:77], v[118:121], v[146:149], v[74:77]
	ds_read_b128 v[102:105], v159 offset:8192
	v_mfma_f32_16x16x32_f16 v[18:21], v[118:121], v[150:153], v[18:21]
	ds_read_b128 v[106:109], v159 offset:10240
	v_mfma_f32_16x16x32_f16 v[26:29], v[118:121], v[154:157], v[26:29]
	ds_read_b128 v[110:113], v161
	v_mfma_f32_16x16x32_f16 v[70:73], v[122:125], v[146:149], v[70:73]
	ds_read_b128 v[114:117], v161 offset:2048
	v_mfma_f32_16x16x32_f16 v[46:49], v[122:125], v[150:153], v[46:49]
	v_mfma_f32_16x16x32_f16 v[240:243], v[122:125], v[154:157], v[240:243]
	s_add_u32 m0, s11, 0xff80
	ds_read_b128 v[118:121], v161 offset:4096
	global_load_lds_dwordx4 v[226:227], off offset:128
	v_mfma_f32_16x16x32_f16 v[66:69], v[126:129], v[146:149], v[66:69]
	ds_read_b128 v[122:125], v161 offset:6144
	v_mfma_f32_16x16x32_f16 v[42:45], v[126:129], v[150:153], v[42:45]
	v_mfma_f32_16x16x32_f16 v[236:239], v[126:129], v[154:157], v[236:239]
	ds_read_b128 v[126:129], v161 offset:8192
	v_mfma_f32_16x16x32_f16 v[62:65], v[130:133], v[146:149], v[62:65]
	v_mfma_f32_16x16x32_f16 v[38:41], v[130:133], v[150:153], v[38:41]
	v_mfma_f32_16x16x32_f16 v[34:37], v[130:133], v[154:157], v[34:37]
	ds_read_b128 v[130:133], v161 offset:10240
	ds_read_b128 v[146:149], v165
	ds_read_b128 v[150:153], v165 offset:2048
	ds_read_b128 v[154:157], v165 offset:4096
	s_waitcnt lgkmcnt(9)
	s_nop 0
	s_add_u32 m0, s11, 0x11f80
	v_mfma_f32_16x16x32_f16 v[82:85], v[86:89], v[134:137], v[82:85]
	global_load_lds_dwordx4 v[220:221], off offset:128
	v_mfma_f32_16x16x32_f16 v[58:61], v[86:89], v[138:141], v[58:61]
	v_mfma_f32_16x16x32_f16 v[14:17], v[86:89], v[142:145], v[14:17]
	v_mfma_f32_16x16x32_f16 v[78:81], v[90:93], v[134:137], v[78:81]
	v_mfma_f32_16x16x32_f16 v[22:25], v[90:93], v[138:141], v[22:25]
	v_mfma_f32_16x16x32_f16 v[30:33], v[90:93], v[142:145], v[30:33]
	s_add_u32 m0, s11, 0x13f80
	v_mfma_f32_16x16x32_f16 v[74:77], v[94:97], v[134:137], v[74:77]
	global_load_lds_dwordx4 v[224:225], off offset:128
	v_mfma_f32_16x16x32_f16 v[18:21], v[94:97], v[138:141], v[18:21]
	v_mfma_f32_16x16x32_f16 v[26:29], v[94:97], v[142:145], v[26:29]
	v_mfma_f32_16x16x32_f16 v[70:73], v[98:101], v[134:137], v[70:73]
	v_mfma_f32_16x16x32_f16 v[46:49], v[98:101], v[138:141], v[46:49]
	v_mfma_f32_16x16x32_f16 v[240:243], v[98:101], v[142:145], v[240:243]
	s_add_u32 m0, s11, 0x15f80
	v_mfma_f32_16x16x32_f16 v[66:69], v[102:105], v[134:137], v[66:69]
	global_load_lds_dwordx4 v[228:229], off offset:128
	v_mfma_f32_16x16x32_f16 v[42:45], v[102:105], v[138:141], v[42:45]
	v_mfma_f32_16x16x32_f16 v[236:239], v[102:105], v[142:145], v[236:239]
	v_mfma_f32_16x16x32_f16 v[62:65], v[106:109], v[134:137], v[62:65]
	v_mfma_f32_16x16x32_f16 v[38:41], v[106:109], v[138:141], v[38:41]
	v_mfma_f32_16x16x32_f16 v[34:37], v[106:109], v[142:145], v[34:37]
	s_waitcnt vmcnt(6) lgkmcnt(0)
	s_barrier
	s_add_u32 m0, s11, 0x17f00
	ds_read_b128 v[134:137], v162
	global_load_lds_dwordx4 v[218:219], off offset:256
	v_mfma_f32_16x16x32_f16 v[82:85], v[110:113], v[146:149], v[82:85]
	ds_read_b128 v[138:141], v162 offset:2048
	v_mfma_f32_16x16x32_f16 v[58:61], v[110:113], v[150:153], v[58:61]
	ds_read_b128 v[142:145], v162 offset:4096
	v_mfma_f32_16x16x32_f16 v[14:17], v[110:113], v[154:157], v[14:17]
	ds_read_b128 v[86:89], v158
	v_mfma_f32_16x16x32_f16 v[78:81], v[114:117], v[146:149], v[78:81]
	ds_read_b128 v[90:93], v158 offset:2048
	v_mfma_f32_16x16x32_f16 v[22:25], v[114:117], v[150:153], v[22:25]
	ds_read_b128 v[94:97], v158 offset:4096
	v_mfma_f32_16x16x32_f16 v[30:33], v[114:117], v[154:157], v[30:33]
	s_add_u32 m0, s11, 0x19f00
	ds_read_b128 v[98:101], v158 offset:6144
	global_load_lds_dwordx4 v[222:223], off offset:256
	v_mfma_f32_16x16x32_f16 v[74:77], v[118:121], v[146:149], v[74:77]
	ds_read_b128 v[102:105], v158 offset:8192
	v_mfma_f32_16x16x32_f16 v[18:21], v[118:121], v[150:153], v[18:21]
	ds_read_b128 v[106:109], v158 offset:10240
	v_mfma_f32_16x16x32_f16 v[26:29], v[118:121], v[154:157], v[26:29]
	ds_read_b128 v[110:113], v160
	v_mfma_f32_16x16x32_f16 v[70:73], v[122:125], v[146:149], v[70:73]
	ds_read_b128 v[114:117], v160 offset:2048
	v_mfma_f32_16x16x32_f16 v[46:49], v[122:125], v[150:153], v[46:49]
	v_mfma_f32_16x16x32_f16 v[240:243], v[122:125], v[154:157], v[240:243]
	s_add_u32 m0, s11, 0x1bf00
	ds_read_b128 v[118:121], v160 offset:4096
	global_load_lds_dwordx4 v[226:227], off offset:256
	v_mfma_f32_16x16x32_f16 v[66:69], v[126:129], v[146:149], v[66:69]
	ds_read_b128 v[122:125], v160 offset:6144
	v_mfma_f32_16x16x32_f16 v[42:45], v[126:129], v[150:153], v[42:45]
	v_mfma_f32_16x16x32_f16 v[236:239], v[126:129], v[154:157], v[236:239]
	ds_read_b128 v[126:129], v160 offset:8192
	v_mfma_f32_16x16x32_f16 v[62:65], v[130:133], v[146:149], v[62:65]
	v_mfma_f32_16x16x32_f16 v[38:41], v[130:133], v[150:153], v[38:41]
	v_mfma_f32_16x16x32_f16 v[34:37], v[130:133], v[154:157], v[34:37]
	ds_read_b128 v[130:133], v160 offset:10240
	ds_read_b128 v[146:149], v164
	ds_read_b128 v[150:153], v164 offset:2048
	ds_read_b128 v[154:157], v164 offset:4096
	v_lshl_add_u64 v[218:219], v[218:219], 0, s[20:21]
	v_lshl_add_u64 v[222:223], v[222:223], 0, s[20:21]
	v_lshl_add_u64 v[226:227], v[226:227], 0, s[20:21]
	v_lshl_add_u64 v[220:221], v[220:221], 0, s[20:21]
	v_lshl_add_u64 v[224:225], v[224:225], 0, s[20:21]
	v_lshl_add_u64 v[228:229], v[228:229], 0, s[20:21]
	s_nop 0
	s_sub_u32 s22, s22, 1
	s_cmp_lg_u32 s22, 0
	s_cbranch_scc1 .Lgemm_N_loop
	s_waitcnt lgkmcnt(9)
	s_nop 0
	s_add_u32 m0, s11, 0x1e080
	v_mfma_f32_16x16x32_f16 v[82:85], v[86:89], v[134:137], v[82:85]
	global_load_lds_dwordx4 v[220:221], off offset:-128
	v_mfma_f32_16x16x32_f16 v[58:61], v[86:89], v[138:141], v[58:61]
	v_mfma_f32_16x16x32_f16 v[14:17], v[86:89], v[142:145], v[14:17]
	v_mfma_f32_16x16x32_f16 v[78:81], v[90:93], v[134:137], v[78:81]
	v_mfma_f32_16x16x32_f16 v[22:25], v[90:93], v[138:141], v[22:25]
	v_mfma_f32_16x16x32_f16 v[30:33], v[90:93], v[142:145], v[30:33]
	s_add_u32 m0, s11, 0x20080
	v_mfma_f32_16x16x32_f16 v[74:77], v[94:97], v[134:137], v[74:77]
	global_load_lds_dwordx4 v[224:225], off offset:-128
	v_mfma_f32_16x16x32_f16 v[18:21], v[94:97], v[138:141], v[18:21]
	v_mfma_f32_16x16x32_f16 v[26:29], v[94:97], v[142:145], v[26:29]
	v_mfma_f32_16x16x32_f16 v[70:73], v[98:101], v[134:137], v[70:73]
	v_mfma_f32_16x16x32_f16 v[46:49], v[98:101], v[138:141], v[46:49]
	v_mfma_f32_16x16x32_f16 v[240:243], v[98:101], v[142:145], v[240:243]
	s_add_u32 m0, s11, 0x22080
	v_mfma_f32_16x16x32_f16 v[66:69], v[102:105], v[134:137], v[66:69]
	global_load_lds_dwordx4 v[228:229], off offset:-128
	v_mfma_f32_16x16x32_f16 v[42:45], v[102:105], v[138:141], v[42:45]
	v_mfma_f32_16x16x32_f16 v[236:239], v[102:105], v[142:145], v[236:239]
	v_mfma_f32_16x16x32_f16 v[62:65], v[106:109], v[134:137], v[62:65]
	v_mfma_f32_16x16x32_f16 v[38:41], v[106:109], v[138:141], v[38:41]
	v_mfma_f32_16x16x32_f16 v[34:37], v[106:109], v[142:145], v[34:37]
	s_waitcnt vmcnt(6) lgkmcnt(0)
	s_barrier
	s_add_u32 m0, s11, 0x0
	s_nop 0
	ds_read_b128 v[134:137], v162 offset:49152
	global_load_lds_dwordx4 v[218:219], off
	v_mfma_f32_16x16x32_f16 v[82:85], v[110:113], v[146:149], v[82:85]
	ds_read_b128 v[138:141], v162 offset:51200
	v_mfma_f32_16x16x32_f16 v[58:61], v[110:113], v[150:153], v[58:61]
	ds_read_b128 v[142:145], v162 offset:53248
	v_mfma_f32_16x16x32_f16 v[14:17], v[110:113], v[154:157], v[14:17]
	ds_read_b128 v[86:89], v158 offset:49152
	v_mfma_f32_16x16x32_f16 v[78:81], v[114:117], v[146:149], v[78:81]
	ds_read_b128 v[90:93], v158 offset:51200
	v_mfma_f32_16x16x32_f16 v[22:25], v[114:117], v[150:153], v[22:25]
	ds_read_b128 v[94:97], v158 offset:53248
	v_mfma_f32_16x16x32_f16 v[30:33], v[114:117], v[154:157], v[30:33]
	s_add_u32 m0, s11, 0x2000
	ds_read_b128 v[98:101], v158 offset:55296
	global_load_lds_dwordx4 v[222:223], off
	v_mfma_f32_16x16x32_f16 v[74:77], v[118:121], v[146:149], v[74:77]
	ds_read_b128 v[102:105], v158 offset:57344
	v_mfma_f32_16x16x32_f16 v[18:21], v[118:121], v[150:153], v[18:21]
	ds_read_b128 v[106:109], v158 offset:59392
	v_mfma_f32_16x16x32_f16 v[26:29], v[118:121], v[154:157], v[26:29]
	ds_read_b128 v[110:113], v160 offset:49152
	v_mfma_f32_16x16x32_f16 v[70:73], v[122:125], v[146:149], v[70:73]
	ds_read_b128 v[114:117], v160 offset:51200
	v_mfma_f32_16x16x32_f16 v[46:49], v[122:125], v[150:153], v[46:49]
	v_mfma_f32_16x16x32_f16 v[240:243], v[122:125], v[154:157], v[240:243]
	s_add_u32 m0, s11, 0x4000
	ds_read_b128 v[118:121], v160 offset:53248
	global_load_lds_dwordx4 v[226:227], off
	v_mfma_f32_16x16x32_f16 v[66:69], v[126:129], v[146:149], v[66:69]
	ds_read_b128 v[122:125], v160 offset:55296
	v_mfma_f32_16x16x32_f16 v[42:45], v[126:129], v[150:153], v[42:45]
	v_mfma_f32_16x16x32_f16 v[236:239], v[126:129], v[154:157], v[236:239]
	ds_read_b128 v[126:129], v160 offset:57344
	v_mfma_f32_16x16x32_f16 v[62:65], v[130:133], v[146:149], v[62:65]
	v_mfma_f32_16x16x32_f16 v[38:41], v[130:133], v[150:153], v[38:41]
	v_mfma_f32_16x16x32_f16 v[34:37], v[130:133], v[154:157], v[34:37]
	ds_read_b128 v[130:133], v160 offset:59392
	ds_read_b128 v[146:149], v164 offset:49152
	ds_read_b128 v[150:153], v164 offset:51200
	ds_read_b128 v[154:157], v164 offset:53248
	s_waitcnt lgkmcnt(9)
	s_nop 0
	s_add_u32 m0, s11, 0x6000
	v_mfma_f32_16x16x32_f16 v[82:85], v[86:89], v[134:137], v[82:85]
	global_load_lds_dwordx4 v[220:221], off
	v_mfma_f32_16x16x32_f16 v[58:61], v[86:89], v[138:141], v[58:61]
	v_mfma_f32_16x16x32_f16 v[14:17], v[86:89], v[142:145], v[14:17]
	v_mfma_f32_16x16x32_f16 v[78:81], v[90:93], v[134:137], v[78:81]
	v_mfma_f32_16x16x32_f16 v[22:25], v[90:93], v[138:141], v[22:25]
	v_mfma_f32_16x16x32_f16 v[30:33], v[90:93], v[142:145], v[30:33]
	s_add_u32 m0, s11, 0x8000
	v_mfma_f32_16x16x32_f16 v[74:77], v[94:97], v[134:137], v[74:77]
	global_load_lds_dwordx4 v[224:225], off
	v_mfma_f32_16x16x32_f16 v[18:21], v[94:97], v[138:141], v[18:21]
	v_mfma_f32_16x16x32_f16 v[26:29], v[94:97], v[142:145], v[26:29]
	v_mfma_f32_16x16x32_f16 v[70:73], v[98:101], v[134:137], v[70:73]
	v_mfma_f32_16x16x32_f16 v[46:49], v[98:101], v[138:141], v[46:49]
	v_mfma_f32_16x16x32_f16 v[240:243], v[98:101], v[142:145], v[240:243]
	s_add_u32 m0, s11, 0xa000
	v_mfma_f32_16x16x32_f16 v[66:69], v[102:105], v[134:137], v[66:69]
	global_load_lds_dwordx4 v[228:229], off
	v_mfma_f32_16x16x32_f16 v[42:45], v[102:105], v[138:141], v[42:45]
	v_mfma_f32_16x16x32_f16 v[236:239], v[102:105], v[142:145], v[236:239]
	v_mfma_f32_16x16x32_f16 v[62:65], v[106:109], v[134:137], v[62:65]
	v_mfma_f32_16x16x32_f16 v[38:41], v[106:109], v[138:141], v[38:41]
	v_mfma_f32_16x16x32_f16 v[34:37], v[106:109], v[142:145], v[34:37]
	s_waitcnt vmcnt(6) lgkmcnt(0)
	s_barrier
	s_lshl_b32 s26, s17, 2
	s_add_u32 s26, s24, s26
	s_addc_u32 s27, s25, 0
	v_lshlrev_b32_e32 v50, 2, v1
	global_load_dword v234, v50, s[26:27]
	global_load_dword v232, v50, s[26:27] offset:64
	global_load_dword v230, v50, s[26:27] offset:128
	ds_read_b128 v[134:137], v163
	v_mfma_f32_16x16x32_f16 v[82:85], v[110:113], v[146:149], v[82:85]
	ds_read_b128 v[138:141], v163 offset:2048
	v_mfma_f32_16x16x32_f16 v[58:61], v[110:113], v[150:153], v[58:61]
	ds_read_b128 v[142:145], v163 offset:4096
	v_mfma_f32_16x16x32_f16 v[14:17], v[110:113], v[154:157], v[14:17]
	ds_read_b128 v[86:89], v159
	v_mfma_f32_16x16x32_f16 v[78:81], v[114:117], v[146:149], v[78:81]
	ds_read_b128 v[90:93], v159 offset:2048
	v_mfma_f32_16x16x32_f16 v[22:25], v[114:117], v[150:153], v[22:25]
	ds_read_b128 v[94:97], v159 offset:4096
	v_mfma_f32_16x16x32_f16 v[30:33], v[114:117], v[154:157], v[30:33]
	ds_read_b128 v[98:101], v159 offset:6144
	v_mfma_f32_16x16x32_f16 v[74:77], v[118:121], v[146:149], v[74:77]
	ds_read_b128 v[102:105], v159 offset:8192
	v_mfma_f32_16x16x32_f16 v[18:21], v[118:121], v[150:153], v[18:21]
	ds_read_b128 v[106:109], v159 offset:10240
	v_mfma_f32_16x16x32_f16 v[26:29], v[118:121], v[154:157], v[26:29]
	ds_read_b128 v[110:113], v161
	v_mfma_f32_16x16x32_f16 v[70:73], v[122:125], v[146:149], v[70:73]
	ds_read_b128 v[114:117], v161 offset:2048
	v_mfma_f32_16x16x32_f16 v[46:49], v[122:125], v[150:153], v[46:49]
	v_mfma_f32_16x16x32_f16 v[240:243], v[122:125], v[154:157], v[240:243]
	ds_read_b128 v[118:121], v161 offset:4096
	v_mfma_f32_16x16x32_f16 v[66:69], v[126:129], v[146:149], v[66:69]
	ds_read_b128 v[122:125], v161 offset:6144
	v_mfma_f32_16x16x32_f16 v[42:45], v[126:129], v[150:153], v[42:45]
	v_mfma_f32_16x16x32_f16 v[236:239], v[126:129], v[154:157], v[236:239]
	ds_read_b128 v[126:129], v161 offset:8192
	v_mfma_f32_16x16x32_f16 v[62:65], v[130:133], v[146:149], v[62:65]
	v_mfma_f32_16x16x32_f16 v[38:41], v[130:133], v[150:153], v[38:41]
	v_mfma_f32_16x16x32_f16 v[34:37], v[130:133], v[154:157], v[34:37]
	ds_read_b128 v[130:133], v161 offset:10240
	ds_read_b128 v[146:149], v165
	ds_read_b128 v[150:153], v165 offset:2048
	ds_read_b128 v[154:157], v165 offset:4096
	s_waitcnt lgkmcnt(9)
	s_nop 0
	v_mfma_f32_16x16x32_f16 v[82:85], v[86:89], v[134:137], v[82:85]
	v_mfma_f32_16x16x32_f16 v[58:61], v[86:89], v[138:141], v[58:61]
	v_mfma_f32_16x16x32_f16 v[14:17], v[86:89], v[142:145], v[14:17]
	v_mfma_f32_16x16x32_f16 v[78:81], v[90:93], v[134:137], v[78:81]
	v_mfma_f32_16x16x32_f16 v[22:25], v[90:93], v[138:141], v[22:25]
	v_mfma_f32_16x16x32_f16 v[30:33], v[90:93], v[142:145], v[30:33]
	v_mfma_f32_16x16x32_f16 v[74:77], v[94:97], v[134:137], v[74:77]
	v_mfma_f32_16x16x32_f16 v[18:21], v[94:97], v[138:141], v[18:21]
	v_mfma_f32_16x16x32_f16 v[26:29], v[94:97], v[142:145], v[26:29]
	v_mfma_f32_16x16x32_f16 v[70:73], v[98:101], v[134:137], v[70:73]
	v_mfma_f32_16x16x32_f16 v[46:49], v[98:101], v[138:141], v[46:49]
	v_mfma_f32_16x16x32_f16 v[240:243], v[98:101], v[142:145], v[240:243]
	v_mfma_f32_16x16x32_f16 v[66:69], v[102:105], v[134:137], v[66:69]
	v_mfma_f32_16x16x32_f16 v[42:45], v[102:105], v[138:141], v[42:45]
	v_mfma_f32_16x16x32_f16 v[236:239], v[102:105], v[142:145], v[236:239]
	v_mfma_f32_16x16x32_f16 v[62:65], v[106:109], v[134:137], v[62:65]
	v_mfma_f32_16x16x32_f16 v[38:41], v[106:109], v[138:141], v[38:41]
	v_mfma_f32_16x16x32_f16 v[34:37], v[106:109], v[142:145], v[34:37]
	s_waitcnt vmcnt(3) lgkmcnt(0)
	s_barrier
	ds_read_b128 v[134:137], v162
	v_mfma_f32_16x16x32_f16 v[82:85], v[110:113], v[146:149], v[82:85]
	ds_read_b128 v[138:141], v162 offset:2048
	v_mfma_f32_16x16x32_f16 v[58:61], v[110:113], v[150:153], v[58:61]
	ds_read_b128 v[142:145], v162 offset:4096
	v_mfma_f32_16x16x32_f16 v[14:17], v[110:113], v[154:157], v[14:17]
	ds_read_b128 v[86:89], v158
	v_mfma_f32_16x16x32_f16 v[78:81], v[114:117], v[146:149], v[78:81]
	ds_read_b128 v[90:93], v158 offset:2048
	v_mfma_f32_16x16x32_f16 v[22:25], v[114:117], v[150:153], v[22:25]
	ds_read_b128 v[94:97], v158 offset:4096
	v_mfma_f32_16x16x32_f16 v[30:33], v[114:117], v[154:157], v[30:33]
	ds_read_b128 v[98:101], v158 offset:6144
	v_mfma_f32_16x16x32_f16 v[74:77], v[118:121], v[146:149], v[74:77]
	ds_read_b128 v[102:105], v158 offset:8192
	v_mfma_f32_16x16x32_f16 v[18:21], v[118:121], v[150:153], v[18:21]
	ds_read_b128 v[106:109], v158 offset:10240
	v_mfma_f32_16x16x32_f16 v[26:29], v[118:121], v[154:157], v[26:29]
	ds_read_b128 v[110:113], v160
	v_mfma_f32_16x16x32_f16 v[70:73], v[122:125], v[146:149], v[70:73]
	ds_read_b128 v[114:117], v160 offset:2048
	v_mfma_f32_16x16x32_f16 v[46:49], v[122:125], v[150:153], v[46:49]
	v_mfma_f32_16x16x32_f16 v[240:243], v[122:125], v[154:157], v[240:243]
	ds_read_b128 v[118:121], v160 offset:4096
	v_mfma_f32_16x16x32_f16 v[66:69], v[126:129], v[146:149], v[66:69]
	ds_read_b128 v[122:125], v160 offset:6144
	v_mfma_f32_16x16x32_f16 v[42:45], v[126:129], v[150:153], v[42:45]
	v_mfma_f32_16x16x32_f16 v[236:239], v[126:129], v[154:157], v[236:239]
	ds_read_b128 v[126:129], v160 offset:8192
	v_mfma_f32_16x16x32_f16 v[62:65], v[130:133], v[146:149], v[62:65]
	v_mfma_f32_16x16x32_f16 v[38:41], v[130:133], v[150:153], v[38:41]
	v_mfma_f32_16x16x32_f16 v[34:37], v[130:133], v[154:157], v[34:37]
	ds_read_b128 v[130:133], v160 offset:10240
	ds_read_b128 v[146:149], v164
	ds_read_b128 v[150:153], v164 offset:2048
	ds_read_b128 v[154:157], v164 offset:4096
	s_waitcnt lgkmcnt(9)
	s_nop 0
	v_mfma_f32_16x16x32_f16 v[82:85], v[86:89], v[134:137], v[82:85]
	v_mfma_f32_16x16x32_f16 v[58:61], v[86:89], v[138:141], v[58:61]
	v_mfma_f32_16x16x32_f16 v[14:17], v[86:89], v[142:145], v[14:17]
	v_mfma_f32_16x16x32_f16 v[78:81], v[90:93], v[134:137], v[78:81]
	v_mfma_f32_16x16x32_f16 v[22:25], v[90:93], v[138:141], v[22:25]
	v_mfma_f32_16x16x32_f16 v[30:33], v[90:93], v[142:145], v[30:33]
	v_mfma_f32_16x16x32_f16 v[74:77], v[94:97], v[134:137], v[74:77]
	v_mfma_f32_16x16x32_f16 v[18:21], v[94:97], v[138:141], v[18:21]
	v_mfma_f32_16x16x32_f16 v[26:29], v[94:97], v[142:145], v[26:29]
	v_mfma_f32_16x16x32_f16 v[70:73], v[98:101], v[134:137], v[70:73]
	v_mfma_f32_16x16x32_f16 v[46:49], v[98:101], v[138:141], v[46:49]
	v_mfma_f32_16x16x32_f16 v[240:243], v[98:101], v[142:145], v[240:243]
	v_mfma_f32_16x16x32_f16 v[66:69], v[102:105], v[134:137], v[66:69]
	v_mfma_f32_16x16x32_f16 v[42:45], v[102:105], v[138:141], v[42:45]
	v_mfma_f32_16x16x32_f16 v[236:239], v[102:105], v[142:145], v[236:239]
	v_mfma_f32_16x16x32_f16 v[62:65], v[106:109], v[134:137], v[62:65]
	v_mfma_f32_16x16x32_f16 v[38:41], v[106:109], v[138:141], v[38:41]
	v_mfma_f32_16x16x32_f16 v[34:37], v[106:109], v[142:145], v[34:37]
	s_waitcnt lgkmcnt(0)
	v_mfma_f32_16x16x32_f16 v[82:85], v[110:113], v[146:149], v[82:85]
	v_mfma_f32_16x16x32_f16 v[58:61], v[110:113], v[150:153], v[58:61]
	v_mfma_f32_16x16x32_f16 v[14:17], v[110:113], v[154:157], v[14:17]
	v_mfma_f32_16x16x32_f16 v[78:81], v[114:117], v[146:149], v[78:81]
	v_mfma_f32_16x16x32_f16 v[22:25], v[114:117], v[150:153], v[22:25]
	v_mfma_f32_16x16x32_f16 v[30:33], v[114:117], v[154:157], v[30:33]
	v_mfma_f32_16x16x32_f16 v[74:77], v[118:121], v[146:149], v[74:77]
	v_mfma_f32_16x16x32_f16 v[18:21], v[118:121], v[150:153], v[18:21]
	v_mfma_f32_16x16x32_f16 v[26:29], v[118:121], v[154:157], v[26:29]
	v_mfma_f32_16x16x32_f16 v[70:73], v[122:125], v[146:149], v[70:73]
	v_mfma_f32_16x16x32_f16 v[46:49], v[122:125], v[150:153], v[46:49]
	v_mfma_f32_16x16x32_f16 v[240:243], v[122:125], v[154:157], v[240:243]
	v_mfma_f32_16x16x32_f16 v[66:69], v[126:129], v[146:149], v[66:69]
	v_mfma_f32_16x16x32_f16 v[42:45], v[126:129], v[150:153], v[42:45]
	v_mfma_f32_16x16x32_f16 v[236:239], v[126:129], v[154:157], v[236:239]
	v_mfma_f32_16x16x32_f16 v[62:65], v[130:133], v[146:149], v[62:65]
	v_mfma_f32_16x16x32_f16 v[38:41], v[130:133], v[150:153], v[38:41]
	v_mfma_f32_16x16x32_f16 v[34:37], v[130:133], v[154:157], v[34:37]
